# first-phase silu(c) loop de-serialised: all eight loads issued before the math (one dependent load per trip before)
# speedup vs baseline: 1.0077x; 1.0077x over previous
; __device__ __forceinline__ void p0_prologue(Frame& F, const Args& a) {
;     ...
;     for (int i = tid; i < NB * D; i += NWAVES * 64) { const float v = c_in[i]; sc[i] = v / (1.f + __expf(-v)); }
.LBB0_14:
	global_load_dword v120, v[2:3], off
	global_load_dword v121, v[2:3], off offset:2048
	v_lshl_add_u64 v[2:3], v[2:3], 0, s[12:13]
	v_lshl_add_u64 v[2:3], v[2:3], 0, s[12:13]
	global_load_dword v122, v[2:3], off
	global_load_dword v123, v[2:3], off offset:2048
	v_lshl_add_u64 v[2:3], v[2:3], 0, s[12:13]
	v_lshl_add_u64 v[2:3], v[2:3], 0, s[12:13]
	global_load_dword v124, v[2:3], off
	global_load_dword v125, v[2:3], off offset:2048
	v_lshl_add_u64 v[2:3], v[2:3], 0, s[12:13]
	v_lshl_add_u64 v[2:3], v[2:3], 0, s[12:13]
	global_load_dword v126, v[2:3], off
	global_load_dword v127, v[2:3], off offset:2048
	s_waitcnt vmcnt(7)
	v_mul_f32_e32 v7, 0xbfb8aa3b, v120
	v_exp_f32_e32 v7, v7
	s_nop 0
	v_add_f32_e32 v7, 1.0, v7
	v_div_scale_f32 v8, s[16:17], v7, v7, v120
	v_rcp_f32_e32 v9, v8
	v_div_scale_f32 v10, vcc, v120, v7, v120
	v_fma_f32 v11, -v8, v9, 1.0
	v_fmac_f32_e32 v9, v11, v9
	v_mul_f32_e32 v11, v10, v9
	v_fma_f32 v12, -v8, v11, v10
	v_fmac_f32_e32 v11, v12, v9
	v_fma_f32 v8, -v8, v11, v10
	v_div_fmas_f32 v8, v8, v9, v11
	v_div_fixup_f32 v1, v8, v7, v120
	ds_write_b32 v6, v1
	s_waitcnt vmcnt(6)
	v_mul_f32_e32 v7, 0xbfb8aa3b, v121
	v_exp_f32_e32 v7, v7
	s_nop 0
	v_add_f32_e32 v7, 1.0, v7
	v_div_scale_f32 v8, s[16:17], v7, v7, v121
	v_rcp_f32_e32 v9, v8
	v_div_scale_f32 v10, vcc, v121, v7, v121
	v_fma_f32 v11, -v8, v9, 1.0
	v_fmac_f32_e32 v9, v11, v9
	v_mul_f32_e32 v11, v10, v9
	v_fma_f32 v12, -v8, v11, v10
	v_fmac_f32_e32 v11, v12, v9
	v_fma_f32 v8, -v8, v11, v10
	v_div_fmas_f32 v8, v8, v9, v11
	v_div_fixup_f32 v1, v8, v7, v121
	ds_write_b32 v6, v1 offset:2048
	s_waitcnt vmcnt(5)
	v_mul_f32_e32 v7, 0xbfb8aa3b, v122
	v_exp_f32_e32 v7, v7
	s_nop 0
	v_add_f32_e32 v7, 1.0, v7
	v_div_scale_f32 v8, s[16:17], v7, v7, v122
	v_rcp_f32_e32 v9, v8
	v_div_scale_f32 v10, vcc, v122, v7, v122
	v_fma_f32 v11, -v8, v9, 1.0
	v_fmac_f32_e32 v9, v11, v9
	v_mul_f32_e32 v11, v10, v9
	v_fma_f32 v12, -v8, v11, v10
	v_fmac_f32_e32 v11, v12, v9
	v_fma_f32 v8, -v8, v11, v10
	v_div_fmas_f32 v8, v8, v9, v11
	v_div_fixup_f32 v1, v8, v7, v122
	ds_write_b32 v6, v1 offset:4096
	s_waitcnt vmcnt(4)
	v_mul_f32_e32 v7, 0xbfb8aa3b, v123
	v_exp_f32_e32 v7, v7
	s_nop 0
	v_add_f32_e32 v7, 1.0, v7
	v_div_scale_f32 v8, s[16:17], v7, v7, v123
	v_rcp_f32_e32 v9, v8
	v_div_scale_f32 v10, vcc, v123, v7, v123
	v_fma_f32 v11, -v8, v9, 1.0
	v_fmac_f32_e32 v9, v11, v9
	v_mul_f32_e32 v11, v10, v9
	v_fma_f32 v12, -v8, v11, v10
	v_fmac_f32_e32 v11, v12, v9
	v_fma_f32 v8, -v8, v11, v10
	v_div_fmas_f32 v8, v8, v9, v11
	v_div_fixup_f32 v1, v8, v7, v123
	ds_write_b32 v6, v1 offset:6144
	s_waitcnt vmcnt(3)
	v_mul_f32_e32 v7, 0xbfb8aa3b, v124
	v_exp_f32_e32 v7, v7
	s_nop 0
	v_add_f32_e32 v7, 1.0, v7
	v_div_scale_f32 v8, s[16:17], v7, v7, v124
	v_rcp_f32_e32 v9, v8
	v_div_scale_f32 v10, vcc, v124, v7, v124
	v_fma_f32 v11, -v8, v9, 1.0
	v_fmac_f32_e32 v9, v11, v9
	v_mul_f32_e32 v11, v10, v9
	v_fma_f32 v12, -v8, v11, v10
	v_fmac_f32_e32 v11, v12, v9
	v_fma_f32 v8, -v8, v11, v10
	v_div_fmas_f32 v8, v8, v9, v11
	v_div_fixup_f32 v1, v8, v7, v124
	ds_write_b32 v6, v1 offset:8192
	s_waitcnt vmcnt(2)
	v_mul_f32_e32 v7, 0xbfb8aa3b, v125
	v_exp_f32_e32 v7, v7
	s_nop 0
	v_add_f32_e32 v7, 1.0, v7
	v_div_scale_f32 v8, s[16:17], v7, v7, v125
	v_rcp_f32_e32 v9, v8
	v_div_scale_f32 v10, vcc, v125, v7, v125
	v_fma_f32 v11, -v8, v9, 1.0
	v_fmac_f32_e32 v9, v11, v9
	v_mul_f32_e32 v11, v10, v9
	v_fma_f32 v12, -v8, v11, v10
	v_fmac_f32_e32 v11, v12, v9
	v_fma_f32 v8, -v8, v11, v10
	v_div_fmas_f32 v8, v8, v9, v11
	v_div_fixup_f32 v1, v8, v7, v125
	ds_write_b32 v6, v1 offset:10240
	s_waitcnt vmcnt(1)
	v_mul_f32_e32 v7, 0xbfb8aa3b, v126
	v_exp_f32_e32 v7, v7
	s_nop 0
	v_add_f32_e32 v7, 1.0, v7
	v_div_scale_f32 v8, s[16:17], v7, v7, v126
	v_rcp_f32_e32 v9, v8
	v_div_scale_f32 v10, vcc, v126, v7, v126
	v_fma_f32 v11, -v8, v9, 1.0
	v_fmac_f32_e32 v9, v11, v9
	v_mul_f32_e32 v11, v10, v9
	v_fma_f32 v12, -v8, v11, v10
	v_fmac_f32_e32 v11, v12, v9
	v_fma_f32 v8, -v8, v11, v10
	v_div_fmas_f32 v8, v8, v9, v11
	v_div_fixup_f32 v1, v8, v7, v126
	ds_write_b32 v6, v1 offset:12288
	s_waitcnt vmcnt(0)
	v_mul_f32_e32 v7, 0xbfb8aa3b, v127
	v_exp_f32_e32 v7, v7
	s_nop 0
	v_add_f32_e32 v7, 1.0, v7
	v_div_scale_f32 v8, s[16:17], v7, v7, v127
	v_rcp_f32_e32 v9, v8
	v_div_scale_f32 v10, vcc, v127, v7, v127
	v_fma_f32 v11, -v8, v9, 1.0
	v_fmac_f32_e32 v9, v11, v9
	v_mul_f32_e32 v11, v10, v9
	v_fma_f32 v12, -v8, v11, v10
	v_fmac_f32_e32 v11, v12, v9
	v_fma_f32 v8, -v8, v11, v10
	v_div_fmas_f32 v8, v8, v9, v11
	v_div_fixup_f32 v1, v8, v7, v127
	ds_write_b32 v6, v1 offset:14336
